# RG-LRU pass 1: x tiles of both items requested together (one exposed memory round trip instead of three), counted waits per LDS piece store
# speedup vs baseline: 1.0004x; 1.0004x over previous
.LBB0_188:
	v_mov_b32_e32 v108, v237
	v_mov_b32_e32 v112, v236
	v_readlane_b32 s2, v253, 10
	v_ashrrev_i32_e32 v109, 31, v108
	v_lshl_add_u64 v[48:49], v[108:109], 4, s[26:27]
	v_add_co_u32_e32 v28, vcc, 0x1000, v48
	v_and_b32_e32 v122, 15, v108
	s_nop 0
	v_addc_co_u32_e32 v29, vcc, 0, v49, vcc
	v_add_co_u32_e32 v44, vcc, 0x2000, v48
	v_lshlrev_b32_e32 v109, 2, v122
	s_nop 0
	v_addc_co_u32_e32 v45, vcc, 0, v49, vcc
	v_or_b32_e32 v110, s28, v109
	v_add_co_u32_e32 v60, vcc, 0x3000, v48
	v_ashrrev_i32_e32 v111, 31, v110
	s_nop 0
	v_addc_co_u32_e32 v61, vcc, 0, v49, vcc
	v_lshlrev_b64 v[64:65], 2, v[110:111]
	global_load_dwordx4 v[0:3], v[48:49], off
	global_load_dwordx4 v[4:7], v[48:49], off offset:1024
	global_load_dwordx4 v[8:11], v[48:49], off offset:2048
	global_load_dwordx4 v[12:15], v[48:49], off offset:3072
	global_load_dwordx4 v[16:19], v[28:29], off
	global_load_dwordx4 v[20:23], v[28:29], off offset:1024
	global_load_dwordx4 v[24:27], v[28:29], off offset:2048
	s_nop 0
	global_load_dwordx4 v[28:31], v[28:29], off offset:3072
	s_nop 0
	global_load_dwordx4 v[32:35], v[44:45], off
	global_load_dwordx4 v[36:39], v[44:45], off offset:1024
	global_load_dwordx4 v[40:43], v[44:45], off offset:2048
	s_nop 0
	global_load_dwordx4 v[44:47], v[44:45], off offset:3072
	s_nop 0
	global_load_dwordx4 v[48:51], v[60:61], off
	global_load_dwordx4 v[52:55], v[60:61], off offset:1024
	global_load_dwordx4 v[56:59], v[60:61], off offset:2048
	s_nop 0
	global_load_dwordx4 v[60:63], v[60:61], off offset:3072
	v_lshl_add_u64 v[66:67], s[56:57], 0, v[64:65]
	global_load_dwordx4 v[88:91], v[66:67], off
	v_lshl_add_u64 v[66:67], s[82:83], 0, v[64:65]
	v_lshl_add_u64 v[64:65], s[54:55], 0, v[64:65]
	global_load_dwordx4 v[80:83], v[66:67], off
	global_load_dwordx4 v[84:87], v[64:65], off
	s_add_i32 s2, s96, s2
	s_cmpk_lt_i32 s2, 0x200
	v_readlane_b32 s3, v253, 11
	s_cselect_b32 s97, s2, -1
	v_lshlrev_b32_e32 v64, 4, v112
	v_and_b32_e32 v134, 0x3f0, v64
	v_lshl_add_u64 v[120:121], s[0:1], 0, v[134:135]
	v_add_u32_e32 v111, 0, v134
	v_add_u32_e32 v134, 0x200, v112
	v_add_u32_e32 v118, 0x400, v112
	v_add_u32_e32 v116, 0x600, v112
	v_add_u32_e32 v114, 0x800, v112
	v_add_u32_e32 v69, 0xa00, v112
	v_add_u32_e32 v70, 0xc00, v112
	v_add_u32_e32 v71, 0xe00, v112
	v_add_u32_e32 v72, 0x1000, v112
	v_ashrrev_i32_e32 v64, 6, v112
	v_ashrrev_i32_e32 v65, 6, v134
	v_ashrrev_i32_e32 v66, 6, v118
	v_ashrrev_i32_e32 v67, 6, v116
	v_ashrrev_i32_e32 v68, 6, v114
	v_ashrrev_i32_e32 v69, 6, v69
	v_ashrrev_i32_e32 v70, 6, v70
	v_ashrrev_i32_e32 v71, 6, v71
	v_ashrrev_i32_e32 v72, 6, v72
	v_add_u32_e32 v113, -3, v64
	v_add_u32_e32 v117, -3, v65
	v_add_u32_e32 v123, -3, v66
	v_add_u32_e32 v125, -3, v67
	v_add_u32_e32 v127, -3, v68
	v_add_u32_e32 v129, -3, v69
	v_add_u32_e32 v131, -3, v70
	v_add_u32_e32 v133, -3, v71
	v_add_u32_e32 v138, -3, v72
	s_movk_i32 s2, 0x10c0
	s_movk_i32 s4, 0xec0
	s_movk_i32 s6, 0xcc0
	s_movk_i32 s8, 0xac0
	s_movk_i32 s10, 0x8c0
	s_movk_i32 s12, 0x6c0
	s_movk_i32 s14, 0x4c0
	s_movk_i32 s16, 0x2c0
	s_movk_i32 s18, 0xc0
	v_min_i32_e32 v115, 63, v113
	v_min_i32_e32 v119, 63, v117
	v_min_i32_e32 v124, 63, v123
	v_min_i32_e32 v126, 63, v125
	v_min_i32_e32 v128, 63, v127
	v_min_i32_e32 v130, 63, v129
	v_min_i32_e32 v132, 63, v131
	v_min_i32_e32 v137, 63, v133
	v_min_i32_e32 v139, 63, v138
	v_cmp_gt_i32_e64 s[2:3], s2, v112
	v_not_b32_e32 v140, v64
	v_mul_lo_u32 v141, v64, s73
	v_cmp_gt_i32_e64 s[4:5], s4, v112
	v_not_b32_e32 v142, v65
	v_mul_lo_u32 v143, v65, s73
	v_cmp_gt_i32_e64 s[6:7], s6, v112
	v_not_b32_e32 v144, v66
	v_mul_lo_u32 v145, v66, s73
	v_cmp_gt_i32_e64 s[8:9], s8, v112
	v_not_b32_e32 v146, v67
	v_mul_lo_u32 v147, v67, s73
	v_cmp_gt_i32_e64 s[10:11], s10, v112
	v_not_b32_e32 v148, v68
	v_mul_lo_u32 v149, v68, s73
	v_cmp_gt_i32_e64 s[12:13], s12, v112
	v_not_b32_e32 v150, v69
	v_mul_lo_u32 v151, v69, s73
	v_cmp_gt_i32_e64 s[14:15], s14, v112
	v_not_b32_e32 v152, v70
	v_mul_lo_u32 v153, v70, s73
	v_cmp_gt_i32_e64 s[16:17], s16, v112
	v_not_b32_e32 v154, v71
	v_mul_lo_u32 v155, v71, s73
	v_cmp_gt_i32_e64 s[18:19], s18, v112
	v_not_b32_e32 v156, v72
	v_mul_lo_u32 v157, v72, s73
	s_lshl_b32 s33, s96, 6
	s_and_b32 s24, s33, 0xfc0
	s_sub_i32 s95, 0, s24
	v_cmp_le_i32_e32 vcc, s95, v113
	s_nop 1
	v_cndmask_b32_e32 v202, 0, v115, vcc
	v_add_u32_e32 v202, s33, v202
	v_lshl_add_u32 v202, v202, 10, v111
	global_load_dwordx4 v[64:67], v202, s[0:1] nt
	v_cmp_le_i32_e32 vcc, s95, v117
	s_nop 1
	v_cndmask_b32_e32 v202, 0, v119, vcc
	v_add_u32_e32 v202, s33, v202
	v_lshl_add_u32 v202, v202, 10, v111
	global_load_dwordx4 v[68:71], v202, s[0:1] nt
	v_cmp_le_i32_e32 vcc, s95, v123
	s_nop 1
	v_cndmask_b32_e32 v202, 0, v124, vcc
	v_add_u32_e32 v202, s33, v202
	v_lshl_add_u32 v202, v202, 10, v111
	global_load_dwordx4 v[72:75], v202, s[0:1] nt
	v_cmp_le_i32_e32 vcc, s95, v125
	s_nop 1
	v_cndmask_b32_e32 v202, 0, v126, vcc
	v_add_u32_e32 v202, s33, v202
	v_lshl_add_u32 v202, v202, 10, v111
	global_load_dwordx4 v[76:79], v202, s[0:1] nt
	v_cmp_le_i32_e32 vcc, s95, v127
	s_nop 1
	v_cndmask_b32_e32 v202, 0, v128, vcc
	v_add_u32_e32 v202, s33, v202
	v_lshl_add_u32 v202, v202, 10, v111
	global_load_dwordx4 v[92:95], v202, s[0:1] nt
	v_cmp_le_i32_e32 vcc, s95, v129
	s_nop 1
	v_cndmask_b32_e32 v202, 0, v130, vcc
	v_add_u32_e32 v202, s33, v202
	v_lshl_add_u32 v202, v202, 10, v111
	global_load_dwordx4 v[96:99], v202, s[0:1] nt
	v_cmp_le_i32_e32 vcc, s95, v131
	s_nop 1
	v_cndmask_b32_e32 v202, 0, v132, vcc
	v_add_u32_e32 v202, s33, v202
	v_lshl_add_u32 v202, v202, 10, v111
	global_load_dwordx4 v[100:103], v202, s[0:1] nt
	v_cmp_le_i32_e32 vcc, s95, v133
	s_nop 1
	v_cndmask_b32_e32 v202, 0, v137, vcc
	v_add_u32_e32 v202, s33, v202
	v_lshl_add_u32 v202, v202, 10, v111
	global_load_dwordx4 v[104:107], v202, s[0:1] nt
	v_cmp_le_i32_e32 vcc, s95, v138
	s_nop 1
	v_cndmask_b32_e32 v202, 0, v139, vcc
	v_add_u32_e32 v202, s33, v202
	v_lshl_add_u32 v202, v202, 10, v111
	global_load_dwordx4 v[160:163], v202, s[0:1] nt
	s_cmp_lt_i32 s97, 0
	s_cbranch_scc1 .Llru_one
	s_lshl_b32 s33, s97, 6
	s_and_b32 s24, s33, 0xfc0
	s_sub_i32 s95, 0, s24
	v_cmp_le_i32_e32 vcc, s95, v113
	s_nop 1
	v_cndmask_b32_e32 v202, 0, v115, vcc
	v_add_u32_e32 v202, s33, v202
	v_lshl_add_u32 v202, v202, 10, v111
	global_load_dwordx4 v[204:207], v202, s[0:1] nt
	v_cmp_le_i32_e32 vcc, s95, v117
	s_nop 1
	v_cndmask_b32_e32 v202, 0, v119, vcc
	v_add_u32_e32 v202, s33, v202
	v_lshl_add_u32 v202, v202, 10, v111
	global_load_dwordx4 v[208:211], v202, s[0:1] nt
	v_cmp_le_i32_e32 vcc, s95, v123
	s_nop 1
	v_cndmask_b32_e32 v202, 0, v124, vcc
	v_add_u32_e32 v202, s33, v202
	v_lshl_add_u32 v202, v202, 10, v111
	global_load_dwordx4 v[212:215], v202, s[0:1] nt
	v_cmp_le_i32_e32 vcc, s95, v125
	s_nop 1
	v_cndmask_b32_e32 v202, 0, v126, vcc
	v_add_u32_e32 v202, s33, v202
	v_lshl_add_u32 v202, v202, 10, v111
	global_load_dwordx4 v[216:219], v202, s[0:1] nt
	v_cmp_le_i32_e32 vcc, s95, v127
	s_nop 1
	v_cndmask_b32_e32 v202, 0, v128, vcc
	v_add_u32_e32 v202, s33, v202
	v_lshl_add_u32 v202, v202, 10, v111
	global_load_dwordx4 v[220:223], v202, s[0:1] nt
	v_cmp_le_i32_e32 vcc, s95, v129
	s_nop 1
	v_cndmask_b32_e32 v202, 0, v130, vcc
	v_add_u32_e32 v202, s33, v202
	v_lshl_add_u32 v202, v202, 10, v111
	global_load_dwordx4 v[224:227], v202, s[0:1] nt
	v_cmp_le_i32_e32 vcc, s95, v131
	s_nop 1
	v_cndmask_b32_e32 v202, 0, v132, vcc
	v_add_u32_e32 v202, s33, v202
	v_lshl_add_u32 v202, v202, 10, v111
	global_load_dwordx4 v[228:231], v202, s[0:1] nt
	v_cmp_le_i32_e32 vcc, s95, v133
	s_nop 1
	v_cndmask_b32_e32 v202, 0, v137, vcc
	v_add_u32_e32 v202, s33, v202
	v_lshl_add_u32 v202, v202, 10, v111
	global_load_dwordx4 v[232:235], v202, s[0:1] nt
	v_cmp_le_i32_e32 vcc, s95, v138
	s_nop 1
	v_cndmask_b32_e32 v202, 0, v139, vcc
	v_add_u32_e32 v202, s33, v202
	v_lshl_add_u32 v202, v202, 10, v111
	global_load_dwordx4 v[240:243], v202, s[0:1] nt
	s_lshl_b32 s33, s96, 6
	s_and_b32 s24, s33, 0xfc0
	s_add_i32 s24, s24, -3
	v_add_u32_e32 v203, s25, v111
	v_cmp_gt_i32_e32 vcc, s24, v140
	v_add_u32_e32 v202, v203, v141
	s_waitcnt vmcnt(17)
	v_cndmask_b32_e32 v64, 0, v64, vcc
	v_cndmask_b32_e32 v65, 0, v65, vcc
	v_cndmask_b32_e32 v66, 0, v66, vcc
	v_cndmask_b32_e32 v67, 0, v67, vcc
	ds_write_b128 v202, v[64:67]
	v_cmp_gt_i32_e32 vcc, s24, v142
	v_add_u32_e32 v202, v203, v143
	s_waitcnt vmcnt(16)
	v_cndmask_b32_e32 v68, 0, v68, vcc
	v_cndmask_b32_e32 v69, 0, v69, vcc
	v_cndmask_b32_e32 v70, 0, v70, vcc
	v_cndmask_b32_e32 v71, 0, v71, vcc
	ds_write_b128 v202, v[68:71]
	v_cmp_gt_i32_e32 vcc, s24, v144
	v_add_u32_e32 v202, v203, v145
	s_waitcnt vmcnt(15)
	v_cndmask_b32_e32 v72, 0, v72, vcc
	v_cndmask_b32_e32 v73, 0, v73, vcc
	v_cndmask_b32_e32 v74, 0, v74, vcc
	v_cndmask_b32_e32 v75, 0, v75, vcc
	ds_write_b128 v202, v[72:75]
	v_cmp_gt_i32_e32 vcc, s24, v146
	v_add_u32_e32 v202, v203, v147
	s_waitcnt vmcnt(14)
	v_cndmask_b32_e32 v76, 0, v76, vcc
	v_cndmask_b32_e32 v77, 0, v77, vcc
	v_cndmask_b32_e32 v78, 0, v78, vcc
	v_cndmask_b32_e32 v79, 0, v79, vcc
	ds_write_b128 v202, v[76:79]
	v_cmp_gt_i32_e32 vcc, s24, v148
	v_add_u32_e32 v202, v203, v149
	s_waitcnt vmcnt(13)
	v_cndmask_b32_e32 v92, 0, v92, vcc
	v_cndmask_b32_e32 v93, 0, v93, vcc
	v_cndmask_b32_e32 v94, 0, v94, vcc
	v_cndmask_b32_e32 v95, 0, v95, vcc
	ds_write_b128 v202, v[92:95]
	v_cmp_gt_i32_e32 vcc, s24, v150
	v_add_u32_e32 v202, v203, v151
	s_waitcnt vmcnt(12)
	v_cndmask_b32_e32 v96, 0, v96, vcc
	v_cndmask_b32_e32 v97, 0, v97, vcc
	v_cndmask_b32_e32 v98, 0, v98, vcc
	v_cndmask_b32_e32 v99, 0, v99, vcc
	ds_write_b128 v202, v[96:99]
	v_cmp_gt_i32_e32 vcc, s24, v152
	v_add_u32_e32 v202, v203, v153
	s_waitcnt vmcnt(11)
	v_cndmask_b32_e32 v100, 0, v100, vcc
	v_cndmask_b32_e32 v101, 0, v101, vcc
	v_cndmask_b32_e32 v102, 0, v102, vcc
	v_cndmask_b32_e32 v103, 0, v103, vcc
	ds_write_b128 v202, v[100:103]
	v_cmp_gt_i32_e32 vcc, s24, v154
	v_add_u32_e32 v202, v203, v155
	s_waitcnt vmcnt(10)
	v_cndmask_b32_e32 v104, 0, v104, vcc
	v_cndmask_b32_e32 v105, 0, v105, vcc
	v_cndmask_b32_e32 v106, 0, v106, vcc
	v_cndmask_b32_e32 v107, 0, v107, vcc
	ds_write_b128 v202, v[104:107]
	s_and_saveexec_b64 s[22:23], s[18:19]
	v_cmp_gt_i32_e32 vcc, s24, v156
	v_add_u32_e32 v202, v203, v157
	s_waitcnt vmcnt(9)
	v_cndmask_b32_e32 v160, 0, v160, vcc
	v_cndmask_b32_e32 v161, 0, v161, vcc
	v_cndmask_b32_e32 v162, 0, v162, vcc
	v_cndmask_b32_e32 v163, 0, v163, vcc
	ds_write_b128 v202, v[160:163]
	s_or_b64 exec, exec, s[22:23]
	s_lshl_b32 s33, s97, 6
	s_and_b32 s24, s33, 0xfc0
	s_add_i32 s24, s24, -3
	v_add_u32_e32 v203, 0x11040, v111
	v_add_u32_e32 v203, s25, v203
	v_cmp_gt_i32_e32 vcc, s24, v140
	v_add_u32_e32 v202, v203, v141
	s_waitcnt vmcnt(8)
	v_cndmask_b32_e32 v204, 0, v204, vcc
	v_cndmask_b32_e32 v205, 0, v205, vcc
	v_cndmask_b32_e32 v206, 0, v206, vcc
	v_cndmask_b32_e32 v207, 0, v207, vcc
	ds_write_b128 v202, v[204:207]
	v_cmp_gt_i32_e32 vcc, s24, v142
	v_add_u32_e32 v202, v203, v143
	s_waitcnt vmcnt(7)
	v_cndmask_b32_e32 v208, 0, v208, vcc
	v_cndmask_b32_e32 v209, 0, v209, vcc
	v_cndmask_b32_e32 v210, 0, v210, vcc
	v_cndmask_b32_e32 v211, 0, v211, vcc
	ds_write_b128 v202, v[208:211]
	v_cmp_gt_i32_e32 vcc, s24, v144
	v_add_u32_e32 v202, v203, v145
	s_waitcnt vmcnt(6)
	v_cndmask_b32_e32 v212, 0, v212, vcc
	v_cndmask_b32_e32 v213, 0, v213, vcc
	v_cndmask_b32_e32 v214, 0, v214, vcc
	v_cndmask_b32_e32 v215, 0, v215, vcc
	ds_write_b128 v202, v[212:215]
	v_cmp_gt_i32_e32 vcc, s24, v146
	v_add_u32_e32 v202, v203, v147
	s_waitcnt vmcnt(5)
	v_cndmask_b32_e32 v216, 0, v216, vcc
	v_cndmask_b32_e32 v217, 0, v217, vcc
	v_cndmask_b32_e32 v218, 0, v218, vcc
	v_cndmask_b32_e32 v219, 0, v219, vcc
	ds_write_b128 v202, v[216:219]
	v_cmp_gt_i32_e32 vcc, s24, v148
	v_add_u32_e32 v202, v203, v149
	s_waitcnt vmcnt(4)
	v_cndmask_b32_e32 v220, 0, v220, vcc
	v_cndmask_b32_e32 v221, 0, v221, vcc
	v_cndmask_b32_e32 v222, 0, v222, vcc
	v_cndmask_b32_e32 v223, 0, v223, vcc
	ds_write_b128 v202, v[220:223]
	v_cmp_gt_i32_e32 vcc, s24, v150
	v_add_u32_e32 v202, v203, v151
	s_waitcnt vmcnt(3)
	v_cndmask_b32_e32 v224, 0, v224, vcc
	v_cndmask_b32_e32 v225, 0, v225, vcc
	v_cndmask_b32_e32 v226, 0, v226, vcc
	v_cndmask_b32_e32 v227, 0, v227, vcc
	ds_write_b128 v202, v[224:227]
	v_cmp_gt_i32_e32 vcc, s24, v152
	v_add_u32_e32 v202, v203, v153
	s_waitcnt vmcnt(2)
	v_cndmask_b32_e32 v228, 0, v228, vcc
	v_cndmask_b32_e32 v229, 0, v229, vcc
	v_cndmask_b32_e32 v230, 0, v230, vcc
	v_cndmask_b32_e32 v231, 0, v231, vcc
	ds_write_b128 v202, v[228:231]
	v_cmp_gt_i32_e32 vcc, s24, v154
	v_add_u32_e32 v202, v203, v155
	s_waitcnt vmcnt(1)
	v_cndmask_b32_e32 v232, 0, v232, vcc
	v_cndmask_b32_e32 v233, 0, v233, vcc
	v_cndmask_b32_e32 v234, 0, v234, vcc
	v_cndmask_b32_e32 v235, 0, v235, vcc
	ds_write_b128 v202, v[232:235]
	s_and_saveexec_b64 s[22:23], s[18:19]
	v_cmp_gt_i32_e32 vcc, s24, v156
	v_add_u32_e32 v202, v203, v157
	s_waitcnt vmcnt(0)
	v_cndmask_b32_e32 v240, 0, v240, vcc
	v_cndmask_b32_e32 v241, 0, v241, vcc
	v_cndmask_b32_e32 v242, 0, v242, vcc
	v_cndmask_b32_e32 v243, 0, v243, vcc
	ds_write_b128 v202, v[240:243]
	s_or_b64 exec, exec, s[22:23]
	s_branch .LBB0_210
.Llru_one:
	s_lshl_b32 s33, s96, 6
	s_and_b32 s24, s33, 0xfc0
	s_add_i32 s24, s24, -3
	v_add_u32_e32 v203, s25, v111
	v_cmp_gt_i32_e32 vcc, s24, v140
	v_add_u32_e32 v202, v203, v141
	s_waitcnt vmcnt(8)
	v_cndmask_b32_e32 v64, 0, v64, vcc
	v_cndmask_b32_e32 v65, 0, v65, vcc
	v_cndmask_b32_e32 v66, 0, v66, vcc
	v_cndmask_b32_e32 v67, 0, v67, vcc
	ds_write_b128 v202, v[64:67]
	v_cmp_gt_i32_e32 vcc, s24, v142
	v_add_u32_e32 v202, v203, v143
	s_waitcnt vmcnt(7)
	v_cndmask_b32_e32 v68, 0, v68, vcc
	v_cndmask_b32_e32 v69, 0, v69, vcc
	v_cndmask_b32_e32 v70, 0, v70, vcc
	v_cndmask_b32_e32 v71, 0, v71, vcc
	ds_write_b128 v202, v[68:71]
	v_cmp_gt_i32_e32 vcc, s24, v144
	v_add_u32_e32 v202, v203, v145
	s_waitcnt vmcnt(6)
	v_cndmask_b32_e32 v72, 0, v72, vcc
	v_cndmask_b32_e32 v73, 0, v73, vcc
	v_cndmask_b32_e32 v74, 0, v74, vcc
	v_cndmask_b32_e32 v75, 0, v75, vcc
	ds_write_b128 v202, v[72:75]
	v_cmp_gt_i32_e32 vcc, s24, v146
	v_add_u32_e32 v202, v203, v147
	s_waitcnt vmcnt(5)
	v_cndmask_b32_e32 v76, 0, v76, vcc
	v_cndmask_b32_e32 v77, 0, v77, vcc
	v_cndmask_b32_e32 v78, 0, v78, vcc
	v_cndmask_b32_e32 v79, 0, v79, vcc
	ds_write_b128 v202, v[76:79]
	v_cmp_gt_i32_e32 vcc, s24, v148
	v_add_u32_e32 v202, v203, v149
	s_waitcnt vmcnt(4)
	v_cndmask_b32_e32 v92, 0, v92, vcc
	v_cndmask_b32_e32 v93, 0, v93, vcc
	v_cndmask_b32_e32 v94, 0, v94, vcc
	v_cndmask_b32_e32 v95, 0, v95, vcc
	ds_write_b128 v202, v[92:95]
	v_cmp_gt_i32_e32 vcc, s24, v150
	v_add_u32_e32 v202, v203, v151
	s_waitcnt vmcnt(3)
	v_cndmask_b32_e32 v96, 0, v96, vcc
	v_cndmask_b32_e32 v97, 0, v97, vcc
	v_cndmask_b32_e32 v98, 0, v98, vcc
	v_cndmask_b32_e32 v99, 0, v99, vcc
	ds_write_b128 v202, v[96:99]
	v_cmp_gt_i32_e32 vcc, s24, v152
	v_add_u32_e32 v202, v203, v153
	s_waitcnt vmcnt(2)
	v_cndmask_b32_e32 v100, 0, v100, vcc
	v_cndmask_b32_e32 v101, 0, v101, vcc
	v_cndmask_b32_e32 v102, 0, v102, vcc
	v_cndmask_b32_e32 v103, 0, v103, vcc
	ds_write_b128 v202, v[100:103]
	v_cmp_gt_i32_e32 vcc, s24, v154
	v_add_u32_e32 v202, v203, v155
	s_waitcnt vmcnt(1)
	v_cndmask_b32_e32 v104, 0, v104, vcc
	v_cndmask_b32_e32 v105, 0, v105, vcc
	v_cndmask_b32_e32 v106, 0, v106, vcc
	v_cndmask_b32_e32 v107, 0, v107, vcc
	ds_write_b128 v202, v[104:107]
	s_and_saveexec_b64 s[22:23], s[18:19]
	v_cmp_gt_i32_e32 vcc, s24, v156
	v_add_u32_e32 v202, v203, v157
	s_waitcnt vmcnt(0)
	v_cndmask_b32_e32 v160, 0, v160, vcc
	v_cndmask_b32_e32 v161, 0, v161, vcc
	v_cndmask_b32_e32 v162, 0, v162, vcc
	v_cndmask_b32_e32 v163, 0, v163, vcc
	ds_write_b128 v202, v[160:163]
	s_or_b64 exec, exec, s[22:23]
